# fox: s_setprio 1/0 also around the PV MFMA cluster
# speedup vs baseline: 1.0018x; 1.0018x over previous
.LBB0_304:
	v_exp_f32_e32 v140, v48
	v_exp_f32_e32 v141, v32
	v_exp_f32_e32 v142, v49
	v_exp_f32_e32 v143, v33
	v_exp_f32_e32 v144, v50
	v_exp_f32_e32 v145, v34
	v_exp_f32_e32 v146, v51
	v_exp_f32_e32 v147, v35
	v_add_f32_e32 v32, v141, v140
	v_exp_f32_e32 v148, v52
	v_exp_f32_e32 v149, v36
	v_add_f32_e32 v32, 0, v32
	v_add_f32_e32 v33, v143, v142
	v_exp_f32_e32 v34, v53
	v_exp_f32_e32 v48, v37
	v_add_f32_e32 v32, v33, v32
	v_add_f32_e32 v33, v145, v144
	v_add_f32_e32 v32, v33, v32
	v_add_f32_e32 v33, v147, v146
	v_add_f32_e32 v35, v33, v32
	v_add_f32_e32 v49, v149, v148
	v_pk_add_f32 v[32:33], v[48:49], v[34:35]
	v_exp_f32_e32 v35, v54
	v_pk_add_f32 v[36:37], v[32:33], v[32:33] op_sel_hi:[0,1]
	v_exp_f32_e32 v49, v38
	v_exp_f32_e32 v36, v55
	v_exp_f32_e32 v50, v39
	v_exp_f32_e32 v52, v41
	v_add_f32_e32 v51, v49, v35
	v_exp_f32_e32 v54, v43
	v_pk_add_f32 v[32:33], v[50:51], v[36:37]
	v_exp_f32_e32 v37, v56
	v_pk_add_f32 v[38:39], v[32:33], v[32:33] op_sel_hi:[0,1]
	v_exp_f32_e32 v51, v40
	v_exp_f32_e32 v38, v57
	v_exp_f32_e32 v56, v45
	v_cvt_pk_bf16_f32 v35, v35, v36
	v_add_f32_e32 v53, v51, v37
	v_pk_add_f32 v[32:33], v[52:53], v[38:39]
	v_exp_f32_e32 v39, v58
	v_pk_add_f32 v[40:41], v[32:33], v[32:33] op_sel_hi:[0,1]
	v_exp_f32_e32 v53, v42
	v_exp_f32_e32 v40, v59
	v_exp_f32_e32 v58, v47
	v_cvt_pk_bf16_f32 v36, v37, v38
	v_add_f32_e32 v55, v53, v39
	v_pk_add_f32 v[32:33], v[54:55], v[40:41]
	v_exp_f32_e32 v41, v60
	v_pk_add_f32 v[42:43], v[32:33], v[32:33] op_sel_hi:[0,1]
	v_exp_f32_e32 v55, v44
	v_exp_f32_e32 v42, v61
	v_cvt_pk_bf16_f32 v37, v39, v40
	v_add_u32_e32 v239, v239, v187
	v_add_f32_e32 v57, v55, v41
	v_pk_add_f32 v[32:33], v[56:57], v[42:43]
	v_exp_f32_e32 v43, v62
	v_pk_add_f32 v[44:45], v[32:33], v[32:33] op_sel_hi:[0,1]
	v_exp_f32_e32 v57, v46
	v_exp_f32_e32 v44, v63
	v_cvt_pk_bf16_f32 v38, v41, v42
	v_cvt_pk_bf16_f32 v42, v149, v48
	v_add_f32_e32 v59, v57, v43
	v_cvt_pk_bf16_f32 v39, v43, v44
	v_cvt_pk_bf16_f32 v43, v49, v50
	ds_read_b64_tr_b16 v[48:49],v241 offset:4096
	v_pk_add_f32 v[32:33], v[58:59], v[44:45]
	v_cvt_pk_bf16_f32 v44, v51, v52
	ds_read_b64_tr_b16 v[50:51],v241 offset:4608
	v_cvt_pk_bf16_f32 v45, v53, v54
	ds_read_b64_tr_b16 v[52:53],v241 offset:5120
	v_cvt_pk_bf16_f32 v46, v55, v56
	ds_read_b64_tr_b16 v[54:55],v241 offset:5632
	v_cvt_pk_bf16_f32 v47, v57, v58
	ds_read_b64_tr_b16 v[56:57],v241 offset:6144
	ds_read_b64_tr_b16 v[58:59],v241 offset:6656
	ds_read_b64_tr_b16 v[60:61],v241 offset:7168
	ds_read_b64_tr_b16 v[62:63],v241 offset:7680
	s_waitcnt lgkmcnt(8)
	v_add_f32_e32 v32, v32, v33
	v_add_f32_e32 v125, v125, v32
	v_cvt_pk_bf16_f32 v32, v140, v142
	v_cvt_pk_bf16_f32 v33, v144, v146
	v_cvt_pk_bf16_f32 v34, v148, v34
	v_cvt_pk_bf16_f32 v40, v141, v143
	v_cvt_pk_bf16_f32 v41, v145, v147
	s_setprio 1
	v_mfma_f32_32x32x16_bf16 v[0:15], v[32:35], v[92:95], v[0:15]
	s_waitcnt lgkmcnt(0)
	v_mfma_f32_32x32x16_bf16 v[0:15], v[36:39], v[88:91], v[0:15]
	v_mfma_f32_32x32x16_bf16 v[0:15], v[40:43], v[84:87], v[0:15]
	v_mfma_f32_32x32x16_bf16 v[0:15], v[44:47], v[80:83], v[0:15]
	v_mfma_f32_32x32x16_bf16 v[16:31], v[32:35], v[48:51], v[16:31]
	s_add_i32 s8, s79, 1
	s_add_i32 s78, s78, 1
	s_and_b32 s79, s8, 3
	s_add_i32 s8, s51, s78
	s_cmp_ge_i32 s8, s75
	v_add_u32_e32 v240, 64, v240
	v_mfma_f32_32x32x16_bf16 v[16:31], v[36:39], v[52:55], v[16:31]
	v_mfma_f32_32x32x16_bf16 v[16:31], v[40:43], v[56:59], v[16:31]
	v_mfma_f32_32x32x16_bf16 v[16:31], v[44:47], v[60:63], v[16:31]
	s_setprio 0
	s_cbranch_scc1 .LBB0_312
	s_nop 0
	v_mov_b32_e32 v242, v243
	s_andn2_b64 vcc, exec, s[28:29]
	s_add_i32 s42, s51, s78
	s_cbranch_vccz .LBB0_283
	s_branch .LBB0_287
